# v49 + instruction-cache warm-up: one wave per workgroup walks 16 execz landing pads in the post-gather code during the gather
# baseline (speedup 1.0000x reference)
.Lg0_start:
	s_add_i32 s53, s8, 7
	s_lshr_b32 s53, s53, 3
	s_mov_b32 s54, s17
	s_add_i32 s55, s17, 4
	s_cmp_ge_u32 s54, s53
	s_cbranch_scc1 .Lg_alldone
	s_mul_i32 s46, s54, 8
	v_add_u32_e32 v220, s46, v221
	v_cmp_gt_u32_e32 vcc, s8, v220
	v_lshlrev_b32_e32 v220, 2, v220
	ds_read_b32 v216, v220
	s_waitcnt lgkmcnt(0)
	v_cndmask_b32_e32 v216, v199, v216, vcc
	s_nop 1
	v_readlane_b32 s50, v216, 0
	s_and_b32 s50, s50, 0xffff
	v_readlane_b32 s40, v216, 0
	s_and_b32 s60, s40, 0xffff
	s_bitcmp1_b32 s40, 31
	s_cselect_b32 s60, 0xffff, s60
	s_bfe_u32 s40, s40, 0xd0010
	s_lshl_b32 s40, s40, 10
	s_add_u32 s42, s32, s40
	s_addc_u32 s43, s33, 0
	global_load_dwordx4 v[66:69], v218, s[42:43] nt
	v_readlane_b32 s40, v216, 1
	s_and_b32 s61, s40, 0xffff
	s_bitcmp1_b32 s40, 31
	s_cselect_b32 s61, 0xffff, s61
	s_bfe_u32 s40, s40, 0xd0010
	s_lshl_b32 s40, s40, 10
	s_add_u32 s42, s32, s40
	s_addc_u32 s43, s33, 0
	global_load_dwordx4 v[70:73], v218, s[42:43] nt
	v_readlane_b32 s40, v216, 2
	s_and_b32 s62, s40, 0xffff
	s_bitcmp1_b32 s40, 31
	s_cselect_b32 s62, 0xffff, s62
	s_bfe_u32 s40, s40, 0xd0010
	s_lshl_b32 s40, s40, 10
	s_add_u32 s42, s32, s40
	s_addc_u32 s43, s33, 0
	global_load_dwordx4 v[74:77], v218, s[42:43] nt
	v_readlane_b32 s40, v216, 3
	s_and_b32 s63, s40, 0xffff
	s_bitcmp1_b32 s40, 31
	s_cselect_b32 s63, 0xffff, s63
	s_bfe_u32 s40, s40, 0xd0010
	s_lshl_b32 s40, s40, 10
	s_add_u32 s42, s32, s40
	s_addc_u32 s43, s33, 0
	global_load_dwordx4 v[78:81], v218, s[42:43] nt
	v_readlane_b32 s40, v216, 4
	s_and_b32 s64, s40, 0xffff
	s_bitcmp1_b32 s40, 31
	s_cselect_b32 s64, 0xffff, s64
	s_bfe_u32 s40, s40, 0xd0010
	s_lshl_b32 s40, s40, 10
	s_add_u32 s42, s32, s40
	s_addc_u32 s43, s33, 0
	global_load_dwordx4 v[82:85], v218, s[42:43] nt
	v_readlane_b32 s40, v216, 5
	s_and_b32 s65, s40, 0xffff
	s_bitcmp1_b32 s40, 31
	s_cselect_b32 s65, 0xffff, s65
	s_bfe_u32 s40, s40, 0xd0010
	s_lshl_b32 s40, s40, 10
	s_add_u32 s42, s32, s40
	s_addc_u32 s43, s33, 0
	global_load_dwordx4 v[86:89], v218, s[42:43] nt
	v_readlane_b32 s40, v216, 6
	s_and_b32 s66, s40, 0xffff
	s_bitcmp1_b32 s40, 31
	s_cselect_b32 s66, 0xffff, s66
	s_bfe_u32 s40, s40, 0xd0010
	s_lshl_b32 s40, s40, 10
	s_add_u32 s42, s32, s40
	s_addc_u32 s43, s33, 0
	global_load_dwordx4 v[90:93], v218, s[42:43] nt
	v_readlane_b32 s40, v216, 7
	s_and_b32 s67, s40, 0xffff
	s_bitcmp1_b32 s40, 31
	s_cselect_b32 s67, 0xffff, s67
	s_bfe_u32 s40, s40, 0xd0010
	s_lshl_b32 s40, s40, 10
	s_add_u32 s42, s32, s40
	s_addc_u32 s43, s33, 0
	global_load_dwordx4 v[94:97], v218, s[42:43] nt
	s_cmp_ge_u32 s55, s53
	s_cbranch_scc1 .Lg0_drainA
	s_mul_i32 s46, s55, 8
	v_add_u32_e32 v220, s46, v221
	v_cmp_gt_u32_e32 vcc, s8, v220
	v_lshlrev_b32_e32 v220, 2, v220
	ds_read_b32 v217, v220
	s_waitcnt lgkmcnt(0)
	v_cndmask_b32_e32 v217, v199, v217, vcc
	s_nop 1
	v_readlane_b32 s40, v217, 0
	s_and_b32 s68, s40, 0xffff
	s_bitcmp1_b32 s40, 31
	s_cselect_b32 s68, 0xffff, s68
	s_bfe_u32 s40, s40, 0xd0010
	s_lshl_b32 s40, s40, 10
	s_add_u32 s42, s32, s40
	s_addc_u32 s43, s33, 0
	global_load_dwordx4 v[98:101], v218, s[42:43] nt
	v_readlane_b32 s40, v217, 1
	s_and_b32 s69, s40, 0xffff
	s_bitcmp1_b32 s40, 31
	s_cselect_b32 s69, 0xffff, s69
	s_bfe_u32 s40, s40, 0xd0010
	s_lshl_b32 s40, s40, 10
	s_add_u32 s42, s32, s40
	s_addc_u32 s43, s33, 0
	global_load_dwordx4 v[102:105], v218, s[42:43] nt
	v_readlane_b32 s40, v217, 2
	s_and_b32 s70, s40, 0xffff
	s_bitcmp1_b32 s40, 31
	s_cselect_b32 s70, 0xffff, s70
	s_bfe_u32 s40, s40, 0xd0010
	s_lshl_b32 s40, s40, 10
	s_add_u32 s42, s32, s40
	s_addc_u32 s43, s33, 0
	global_load_dwordx4 v[106:109], v218, s[42:43] nt
	v_readlane_b32 s40, v217, 3
	s_and_b32 s71, s40, 0xffff
	s_bitcmp1_b32 s40, 31
	s_cselect_b32 s71, 0xffff, s71
	s_bfe_u32 s40, s40, 0xd0010
	s_lshl_b32 s40, s40, 10
	s_add_u32 s42, s32, s40
	s_addc_u32 s43, s33, 0
	global_load_dwordx4 v[110:113], v218, s[42:43] nt
	v_readlane_b32 s40, v217, 4
	s_and_b32 s72, s40, 0xffff
	s_bitcmp1_b32 s40, 31
	s_cselect_b32 s72, 0xffff, s72
	s_bfe_u32 s40, s40, 0xd0010
	s_lshl_b32 s40, s40, 10
	s_add_u32 s42, s32, s40
	s_addc_u32 s43, s33, 0
	global_load_dwordx4 v[114:117], v218, s[42:43] nt
	v_readlane_b32 s40, v217, 5
	s_and_b32 s73, s40, 0xffff
	s_bitcmp1_b32 s40, 31
	s_cselect_b32 s73, 0xffff, s73
	s_bfe_u32 s40, s40, 0xd0010
	s_lshl_b32 s40, s40, 10
	s_add_u32 s42, s32, s40
	s_addc_u32 s43, s33, 0
	global_load_dwordx4 v[118:121], v218, s[42:43] nt
	v_readlane_b32 s40, v217, 6
	s_and_b32 s74, s40, 0xffff
	s_bitcmp1_b32 s40, 31
	s_cselect_b32 s74, 0xffff, s74
	s_bfe_u32 s40, s40, 0xd0010
	s_lshl_b32 s40, s40, 10
	s_add_u32 s42, s32, s40
	s_addc_u32 s43, s33, 0
	global_load_dwordx4 v[122:125], v218, s[42:43] nt
	v_readlane_b32 s40, v217, 7
	s_and_b32 s75, s40, 0xffff
	s_bitcmp1_b32 s40, 31
	s_cselect_b32 s75, 0xffff, s75
	s_bfe_u32 s40, s40, 0xd0010
	s_lshl_b32 s40, s40, 10
	s_add_u32 s42, s32, s40
	s_addc_u32 s43, s33, 0
	global_load_dwordx4 v[126:129], v218, s[42:43] nt
	s_cmp_lg_u32 s17, 3
	s_cbranch_scc1 .Lg0_loop
	s_mov_b64 s[94:95], exec
	s_mov_b64 exec, 0
	s_branch .Lpad_0
.Lwret_0:
	s_branch .Lpad_1
.Lwret_1:
	s_branch .Lpad_2
.Lwret_2:
	s_branch .Lpad_3
.Lwret_3:
	s_branch .Lpad_4
.Lwret_4:
	s_branch .Lpad_5
.Lwret_5:
	s_branch .Lpad_6
.Lwret_6:
	s_branch .Lpad_7
.Lwret_7:
	s_branch .Lpad_8
.Lwret_8:
	s_branch .Lpad_9
.Lwret_9:
	s_branch .Lpad_10
.Lwret_10:
	s_branch .Lpad_11
.Lwret_11:
	s_branch .Lpad_12
.Lwret_12:
	s_branch .Lpad_13
.Lwret_13:
	s_branch .Lpad_14
.Lwret_14:
	s_branch .Lpad_15
.Lwret_15:
	s_mov_b64 exec, s[94:95]

.Lpad_0:
	s_cbranch_execz .Lwret_0
	ds_read_b32 v66, v66
	v_mul_u32_u24_e32 v68, 0x102, v67
	v_lshlrev_b32_e32 v72, 3, v68
	s_waitcnt lgkmcnt(0)
	v_max_i32_e32 v66, 1, v66
	v_cvt_f32_u32_e32 v66, v66
	v_div_scale_f32 v69, s[0:1], v66, v66, 1.0
	v_rcp_f32_e32 v70, v69
	v_div_scale_f32 v68, vcc, 1.0, v66, 1.0
	v_fma_f32 v71, -v69, v70, 1.0
	v_fmac_f32_e32 v70, v71, v70
	v_mul_f32_e32 v71, v68, v70
	v_fma_f32 v73, -v69, v71, v68
	v_fmac_f32_e32 v71, v73, v70
	v_fma_f32 v68, -v69, v71, v68
	v_div_fmas_f32 v73, v68, v70, v71
	v_lshl_add_u32 v68, v138, 3, v72
	v_add_u32_e32 v76, 0x8000, v68
	ds_read2_b64 v[68:71], v76 offset1:16
	v_div_fixup_f32 v77, v73, v66, 1.0
	v_mul_i32_i24_e32 v73, 0xfffffbf8, v67
	v_lshlrev_b32_e32 v66, 2, v138
	v_add3_u32 v78, v72, v73, v66
	ds_read2_b64 v[72:75], v76 offset0:32 offset1:48
	s_waitcnt lgkmcnt(1)
	v_cvt_f32_f64_e32 v68, v[68:69]
	v_cvt_f32_f64_e32 v69, v[70:71]
	v_mul_f32_e32 v68, v77, v68
	v_mul_f32_e32 v69, v77, v69
	v_fma_f32 v79, v68, v68, 0
	ds_write2_b32 v78, v68, v69 offset1:16
	s_waitcnt lgkmcnt(1)
	v_cvt_f32_f64_e32 v68, v[72:73]
	v_fmac_f32_e32 v79, v69, v69
	v_mul_f32_e32 v72, v77, v68
	ds_read2_b64 v[68:71], v76 offset0:64 offset1:80
	v_cvt_f32_f64_e32 v73, v[74:75]
	v_fmac_f32_e32 v79, v72, v72
	v_mul_f32_e32 v73, v77, v73
	v_fmac_f32_e32 v79, v73, v73
	ds_write2_b32 v78, v72, v73 offset0:32 offset1:48
	ds_read2_b64 v[72:75], v76 offset0:96 offset1:112
	s_waitcnt lgkmcnt(2)
	v_cvt_f32_f64_e32 v68, v[68:69]
	v_cvt_f32_f64_e32 v69, v[70:71]
	v_mul_f32_e32 v68, v77, v68
	v_mul_f32_e32 v69, v77, v69
	v_fmac_f32_e32 v79, v68, v68
	ds_write2_b32 v78, v68, v69 offset0:64 offset1:80
	s_waitcnt lgkmcnt(1)
	v_cvt_f32_f64_e32 v68, v[72:73]
	v_fmac_f32_e32 v79, v69, v69
	v_mul_f32_e32 v72, v77, v68
	ds_read2_b64 v[68:71], v76 offset0:128 offset1:144
	v_cvt_f32_f64_e32 v73, v[74:75]
	v_fmac_f32_e32 v79, v72, v72
	v_mul_f32_e32 v73, v77, v73
	v_fmac_f32_e32 v79, v73, v73
	ds_write2_b32 v78, v72, v73 offset0:96 offset1:112
	ds_read2_b64 v[72:75], v76 offset0:160 offset1:176
	s_waitcnt lgkmcnt(2)
	v_cvt_f32_f64_e32 v68, v[68:69]
	v_cvt_f32_f64_e32 v69, v[70:71]
	v_mul_f32_e32 v68, v77, v68
	v_mul_f32_e32 v69, v77, v69
	v_fmac_f32_e32 v79, v68, v68
	ds_write2_b32 v78, v68, v69 offset0:128 offset1:144
	s_waitcnt lgkmcnt(1)
	v_cvt_f32_f64_e32 v68, v[72:73]
	v_fmac_f32_e32 v79, v69, v69
	v_mul_f32_e32 v72, v77, v68
	ds_read2_b64 v[68:71], v76 offset0:192 offset1:208
	v_cvt_f32_f64_e32 v73, v[74:75]
	v_fmac_f32_e32 v79, v72, v72
	v_mul_f32_e32 v73, v77, v73
	v_fmac_f32_e32 v79, v73, v73
	ds_write2_b32 v78, v72, v73 offset0:160 offset1:176
	ds_read2_b64 v[72:75], v76 offset0:224 offset1:240
	s_waitcnt lgkmcnt(2)
	v_cvt_f32_f64_e32 v68, v[68:69]
	v_cvt_f32_f64_e32 v69, v[70:71]
	v_mul_f32_e32 v68, v77, v68
	v_mul_f32_e32 v69, v77, v69
	v_fmac_f32_e32 v79, v68, v68
	ds_write2_b32 v78, v68, v69 offset0:192 offset1:208
	s_waitcnt lgkmcnt(1)
	v_cvt_f32_f64_e32 v68, v[72:73]
	v_fmac_f32_e32 v79, v69, v69
	v_mul_f32_e32 v68, v77, v68
	v_cvt_f32_f64_e32 v69, v[74:75]
	v_fmac_f32_e32 v79, v68, v68
	v_mul_f32_e32 v69, v77, v69
	v_fmac_f32_e32 v79, v69, v69
	ds_write2_b32 v78, v68, v69 offset0:224 offset1:240
	v_cmp_eq_u32_e32 vcc, 0, v138
	v_add_f32_dpp v68, v79, v79 quad_perm:[1,0,3,2] row_mask:0xf bank_mask:0xf bound_ctrl:1
	s_nop 1
	v_add_f32_dpp v68, v68, v68 quad_perm:[2,3,0,1] row_mask:0xf bank_mask:0xf bound_ctrl:1
	s_nop 1
	v_add_f32_dpp v68, v68, v68 row_half_mirror row_mask:0xf bank_mask:0xf bound_ctrl:1
	s_nop 1
	v_mov_b32_dpp v69, v68 row_mirror row_mask:0xf bank_mask:0xf bound_ctrl:1
	s_and_saveexec_b64 s[0:1], vcc
	v_mov_b32_e32 v70, 0x11200
	v_lshl_or_b32 v67, v67, 2, v70
	v_add_f32_e32 v68, v68, v69
	ds_write_b32 v67, v68
	s_or_b64 exec, exec, s[0:1]
	v_lshlrev_b32_e32 v67, 2, v140
	s_movk_i32 s0, 0x408
	v_mad_u32_u24 v67, v138, s0, v67
	s_waitcnt lgkmcnt(0)
	s_barrier
.Lpad_1:
	s_cbranch_execz .Lwret_1
	ds_read2_b32 v[68:69], v67 offset1:4
	ds_read2_b32 v[70:71], v67 offset0:64 offset1:68
	ds_read2_b32 v[72:73], v67 offset0:192 offset1:196
	s_lshl_b32 s29, s17, 2
	s_lshl_b32 s0, s24, 2
	s_waitcnt lgkmcnt(2)
	v_mfma_f32_16x16x4_f32 a[0:3], v68, v62, 0
	s_add_i32 s0, s0, 0x10100
	s_waitcnt lgkmcnt(1)
	v_mfma_f32_16x16x4_f32 a[4:7], v70, v63, 0
	ds_read2_b32 v[62:63], v67 offset0:128 offset1:132
	s_waitcnt lgkmcnt(0)
	v_mfma_f32_16x16x4_f32 a[0:3], v62, v64, a[0:3]
	v_mfma_f32_16x16x4_f32 a[4:7], v72, v65, a[4:7]
	v_mfma_f32_16x16x4_f32 a[0:3], v69, v58, a[0:3]
	v_mfma_f32_16x16x4_f32 a[4:7], v71, v59, a[4:7]
	ds_read2_b32 v[58:59], v67 offset0:8 offset1:12
	v_mfma_f32_16x16x4_f32 a[0:3], v63, v60, a[0:3]
	ds_read2_b32 v[62:63], v67 offset0:200 offset1:204
	v_mfma_f32_16x16x4_f32 a[4:7], v73, v61, a[4:7]
	ds_read2_b32 v[60:61], v67 offset0:72 offset1:76
	s_waitcnt lgkmcnt(2)
	v_mfma_f32_16x16x4_f32 a[0:3], v58, v54, a[0:3]
	s_waitcnt lgkmcnt(0)
	v_mfma_f32_16x16x4_f32 a[4:7], v60, v55, a[4:7]
	ds_read2_b32 v[54:55], v67 offset0:136 offset1:140
	s_waitcnt lgkmcnt(0)
	v_mfma_f32_16x16x4_f32 a[0:3], v54, v56, a[0:3]
	v_mfma_f32_16x16x4_f32 a[4:7], v62, v57, a[4:7]
	v_mfma_f32_16x16x4_f32 a[0:3], v59, v50, a[0:3]
	v_mfma_f32_16x16x4_f32 a[4:7], v61, v51, a[4:7]
	ds_read2_b32 v[50:51], v67 offset0:16 offset1:20
	v_mfma_f32_16x16x4_f32 a[0:3], v55, v52, a[0:3]
	ds_read2_b32 v[54:55], v67 offset0:208 offset1:212
	v_mfma_f32_16x16x4_f32 a[4:7], v63, v53, a[4:7]
.Lpad_2:
	s_cbranch_execz .Lwret_2
	ds_read2_b32 v[52:53], v67 offset0:80 offset1:84
	s_waitcnt lgkmcnt(2)
	v_mfma_f32_16x16x4_f32 a[0:3], v50, v46, a[0:3]
	s_waitcnt lgkmcnt(0)
	v_mfma_f32_16x16x4_f32 a[4:7], v52, v47, a[4:7]
	ds_read2_b32 v[46:47], v67 offset0:144 offset1:148
	s_waitcnt lgkmcnt(0)
	v_mfma_f32_16x16x4_f32 a[0:3], v46, v48, a[0:3]
	v_mfma_f32_16x16x4_f32 a[4:7], v54, v49, a[4:7]
	v_mfma_f32_16x16x4_f32 a[0:3], v51, v42, a[0:3]
	v_mfma_f32_16x16x4_f32 a[4:7], v53, v43, a[4:7]
	ds_read2_b32 v[42:43], v67 offset0:24 offset1:28
	v_mfma_f32_16x16x4_f32 a[0:3], v47, v44, a[0:3]
	ds_read2_b32 v[46:47], v67 offset0:216 offset1:220
	v_mfma_f32_16x16x4_f32 a[4:7], v55, v45, a[4:7]
	ds_read2_b32 v[44:45], v67 offset0:88 offset1:92
	s_waitcnt lgkmcnt(2)
	v_mfma_f32_16x16x4_f32 a[0:3], v42, v38, a[0:3]
	s_waitcnt lgkmcnt(0)
	v_mfma_f32_16x16x4_f32 a[4:7], v44, v39, a[4:7]
	ds_read2_b32 v[38:39], v67 offset0:152 offset1:156
	s_waitcnt lgkmcnt(0)
	v_mfma_f32_16x16x4_f32 a[0:3], v38, v40, a[0:3]
	v_mfma_f32_16x16x4_f32 a[4:7], v46, v41, a[4:7]
	v_mfma_f32_16x16x4_f32 a[0:3], v43, v34, a[0:3]
	v_mfma_f32_16x16x4_f32 a[4:7], v45, v35, a[4:7]
	ds_read2_b32 v[34:35], v67 offset0:32 offset1:36
	v_mfma_f32_16x16x4_f32 a[0:3], v39, v36, a[0:3]
	ds_read2_b32 v[38:39], v67 offset0:224 offset1:228
	v_mfma_f32_16x16x4_f32 a[4:7], v47, v37, a[4:7]
	ds_read2_b32 v[36:37], v67 offset0:96 offset1:100
	s_waitcnt lgkmcnt(2)
	v_mfma_f32_16x16x4_f32 a[0:3], v34, v30, a[0:3]
	s_waitcnt lgkmcnt(0)
	v_mfma_f32_16x16x4_f32 a[4:7], v36, v31, a[4:7]
	ds_read2_b32 v[30:31], v67 offset0:160 offset1:164
	s_waitcnt lgkmcnt(0)
	v_mfma_f32_16x16x4_f32 a[0:3], v30, v32, a[0:3]
	v_mfma_f32_16x16x4_f32 a[4:7], v38, v33, a[4:7]
	v_mfma_f32_16x16x4_f32 a[0:3], v35, v26, a[0:3]
	v_mfma_f32_16x16x4_f32 a[4:7], v37, v27, a[4:7]
	ds_read2_b32 v[26:27], v67 offset0:40 offset1:44
	v_mfma_f32_16x16x4_f32 a[0:3], v31, v28, a[0:3]
	ds_read2_b32 v[30:31], v67 offset0:232 offset1:236
	v_mfma_f32_16x16x4_f32 a[4:7], v39, v29, a[4:7]
	ds_read2_b32 v[28:29], v67 offset0:104 offset1:108
	s_waitcnt lgkmcnt(2)
	v_mfma_f32_16x16x4_f32 a[0:3], v26, v22, a[0:3]
	s_waitcnt lgkmcnt(0)
	v_mfma_f32_16x16x4_f32 a[4:7], v28, v23, a[4:7]
	ds_read2_b32 v[22:23], v67 offset0:168 offset1:172
	s_waitcnt lgkmcnt(0)
	v_mfma_f32_16x16x4_f32 a[0:3], v22, v24, a[0:3]
	v_mfma_f32_16x16x4_f32 a[4:7], v30, v25, a[4:7]
	v_mfma_f32_16x16x4_f32 a[0:3], v27, v18, a[0:3]
	v_mfma_f32_16x16x4_f32 a[4:7], v29, v19, a[4:7]
	ds_read2_b32 v[18:19], v67 offset0:48 offset1:52
	v_mfma_f32_16x16x4_f32 a[0:3], v23, v20, a[0:3]
	ds_read2_b32 v[22:23], v67 offset0:240 offset1:244
	v_mfma_f32_16x16x4_f32 a[4:7], v31, v21, a[4:7]
.Lpad_3:
	s_cbranch_execz .Lwret_3
	ds_read2_b32 v[20:21], v67 offset0:112 offset1:116
	s_waitcnt lgkmcnt(2)
	v_mfma_f32_16x16x4_f32 a[0:3], v18, v14, a[0:3]
	s_waitcnt lgkmcnt(0)
	v_mfma_f32_16x16x4_f32 a[4:7], v20, v15, a[4:7]
	ds_read2_b32 v[14:15], v67 offset0:176 offset1:180
	s_waitcnt lgkmcnt(0)
	v_mfma_f32_16x16x4_f32 a[0:3], v14, v16, a[0:3]
	v_mfma_f32_16x16x4_f32 a[4:7], v22, v17, a[4:7]
	v_mfma_f32_16x16x4_f32 a[0:3], v19, v10, a[0:3]
	v_mfma_f32_16x16x4_f32 a[4:7], v21, v11, a[4:7]
	ds_read2_b32 v[10:11], v67 offset0:56 offset1:60
	v_mfma_f32_16x16x4_f32 a[0:3], v15, v12, a[0:3]
	ds_read2_b32 v[14:15], v67 offset0:248 offset1:252
	v_mfma_f32_16x16x4_f32 a[4:7], v23, v13, a[4:7]
	ds_read2_b32 v[12:13], v67 offset0:120 offset1:124
	s_waitcnt lgkmcnt(2)
	v_mfma_f32_16x16x4_f32 a[0:3], v10, v6, a[0:3]
	s_waitcnt lgkmcnt(0)
	v_mfma_f32_16x16x4_f32 a[4:7], v12, v7, a[4:7]
	ds_read2_b32 v[6:7], v67 offset0:184 offset1:188
	s_waitcnt lgkmcnt(0)
	v_mfma_f32_16x16x4_f32 a[0:3], v6, v8, a[0:3]
	v_mfma_f32_16x16x4_f32 a[4:7], v14, v9, a[4:7]
	v_mfma_f32_16x16x4_f32 a[0:3], v11, v2, a[0:3]
	v_mov_b32_e32 v2, 0x11300
	v_lshl_add_u32 v2, v134, 2, v2
	ds_read_b32 v2, v2
	v_mfma_f32_16x16x4_f32 a[4:7], v13, v3, a[4:7]
	v_lshlrev_b32_e32 v3, 10, v140
	v_add3_u32 v3, s0, v66, v3
	v_mfma_f32_16x16x4_f32 a[0:3], v7, v4, a[0:3]
	v_or_b32_e32 v7, s29, v140
	v_lshl_or_b32 v4, v7, 8, v66
	v_add_u32_e32 v4, 0x10100, v4
	v_mfma_f32_16x16x4_f32 a[4:7], v15, v5, a[4:7]
	s_nop 9
	v_accvgpr_read_b32 v5, a0
	v_accvgpr_read_b32 v6, a1
	v_accvgpr_read_b32 v8, a2
	v_accvgpr_read_b32 v9, a3
	v_accvgpr_read_b32 v70, a4
	v_accvgpr_read_b32 v71, a5
	v_accvgpr_read_b32 v72, a6
	v_accvgpr_read_b32 v73, a7
	v_add_f32_e32 v5, v5, v70
	v_add_f32_e32 v6, v6, v71
	v_add_f32_e32 v8, v8, v72
	v_add_f32_e32 v9, v9, v73
	s_waitcnt lgkmcnt(0)
	v_fma_f32 v5, -2.0, v5, v2
	v_fma_f32 v6, -2.0, v6, v2
	v_fma_f32 v8, -2.0, v8, v2
	v_fmac_f32_e32 v2, -2.0, v9
	ds_write2st64_b32 v3, v5, v6 offset1:1
	ds_write2st64_b32 v3, v8, v2 offset0:2 offset1:3
	s_waitcnt lgkmcnt(0)
	s_barrier
.Lpad_4:
	s_cbranch_execz .Lwret_4
	ds_read2_b32 v[2:3], v4 offset1:16
	ds_read2_b32 v[4:5], v4 offset0:32 offset1:48
	v_or_b32_e32 v6, 16, v138
	v_or_b32_e32 v8, 32, v138
	v_or_b32_e32 v9, 48, v138
	s_waitcnt lgkmcnt(1)
	v_cmp_lt_f32_e32 vcc, v3, v2
	s_nop 1
	v_cndmask_b32_e32 v10, v2, v3, vcc
	v_cndmask_b32_e32 v6, v138, v6, vcc
	s_waitcnt lgkmcnt(0)
	v_cmp_lt_f32_e32 vcc, v4, v10
	s_nop 1
	v_cndmask_b32_e32 v10, v10, v4, vcc
	v_cndmask_b32_e32 v8, v6, v8, vcc
	v_cmp_lt_f32_e32 vcc, v5, v10
	s_nop 1
	v_cndmask_b32_e32 v6, v10, v5, vcc
	v_cndmask_b32_e32 v14, v8, v9, vcc
	s_nop 0
	v_mov_b32_dpp v9, v6 quad_perm:[1,0,3,2] row_mask:0xf bank_mask:0xf bound_ctrl:1
	v_mov_b32_dpp v8, v14 quad_perm:[1,0,3,2] row_mask:0xf bank_mask:0xf bound_ctrl:1
	v_cmp_gt_f32_e64 s[4:5], v6, v9
	v_cmp_ngt_f32_e32 vcc, v6, v9
	s_and_saveexec_b64 s[6:7], vcc
	v_cmp_eq_f32_e32 vcc, v6, v9
	v_cmp_lt_i32_e64 s[0:1], v8, v14
	s_and_b64 s[0:1], vcc, s[0:1]
	s_andn2_b64 s[4:5], s[4:5], exec
	s_and_b64 s[0:1], s[0:1], exec
	s_or_b64 s[4:5], s[4:5], s[0:1]
	s_or_b64 exec, exec, s[6:7]
	s_and_saveexec_b64 s[0:1], s[4:5]
	v_mov_b32_e32 v6, v9
	v_mov_b32_e32 v14, v8
	s_or_b64 exec, exec, s[0:1]
	v_mov_b32_dpp v9, v6 quad_perm:[2,3,0,1] row_mask:0xf bank_mask:0xf bound_ctrl:1
	v_mov_b32_dpp v8, v14 quad_perm:[2,3,0,1] row_mask:0xf bank_mask:0xf bound_ctrl:1
	v_cmp_gt_f32_e64 s[4:5], v6, v9
	v_cmp_ngt_f32_e32 vcc, v6, v9
	s_and_saveexec_b64 s[6:7], vcc
	v_cmp_eq_f32_e32 vcc, v6, v9
	v_cmp_lt_i32_e64 s[0:1], v8, v14
	s_and_b64 s[0:1], vcc, s[0:1]
	s_andn2_b64 s[4:5], s[4:5], exec
	s_and_b64 s[0:1], s[0:1], exec
	s_or_b64 s[4:5], s[4:5], s[0:1]
	s_or_b64 exec, exec, s[6:7]
	s_and_saveexec_b64 s[0:1], s[4:5]
	v_mov_b32_e32 v6, v9
	v_mov_b32_e32 v14, v8
	s_or_b64 exec, exec, s[0:1]
.Lpad_5:
	s_cbranch_execz .Lwret_5
	v_mov_b32_dpp v9, v6 row_half_mirror row_mask:0xf bank_mask:0xf bound_ctrl:1
	v_mov_b32_dpp v8, v14 row_half_mirror row_mask:0xf bank_mask:0xf bound_ctrl:1
	v_cmp_gt_f32_e64 s[4:5], v6, v9
	v_cmp_ngt_f32_e32 vcc, v6, v9
	s_and_saveexec_b64 s[6:7], vcc
	v_cmp_eq_f32_e32 vcc, v6, v9
	v_cmp_lt_i32_e64 s[0:1], v8, v14
	s_and_b64 s[0:1], vcc, s[0:1]
	s_andn2_b64 s[4:5], s[4:5], exec
	s_and_b64 s[0:1], s[0:1], exec
	s_or_b64 s[4:5], s[4:5], s[0:1]
	s_or_b64 exec, exec, s[6:7]
	s_and_saveexec_b64 s[0:1], s[4:5]
	v_mov_b32_e32 v6, v9
	v_mov_b32_e32 v14, v8
	s_or_b64 exec, exec, s[0:1]
	v_mov_b32_dpp v8, v6 row_mirror row_mask:0xf bank_mask:0xf bound_ctrl:1
	v_mov_b32_dpp v9, v14 row_mirror row_mask:0xf bank_mask:0xf bound_ctrl:1
	v_cmp_gt_f32_e64 s[4:5], v6, v8
	v_cmp_ngt_f32_e32 vcc, v6, v8
	s_and_saveexec_b64 s[6:7], vcc
	v_cmp_eq_f32_e32 vcc, v6, v8
	v_cmp_lt_i32_e64 s[0:1], v9, v14
	s_and_b64 s[0:1], vcc, s[0:1]
	s_andn2_b64 s[4:5], s[4:5], exec
	s_and_b64 s[0:1], s[0:1], exec
	s_or_b64 s[4:5], s[4:5], s[0:1]
	s_or_b64 exec, exec, s[6:7]
	s_and_saveexec_b64 s[0:1], s[4:5]
	v_mov_b32_e32 v6, v8
	v_mov_b32_e32 v14, v9
	s_or_b64 exec, exec, s[0:1]
.Lpad_6:
	s_cbranch_execz .Lwret_6
	v_mov_b32_e32 v8, 0x11300
	v_lshl_or_b32 v8, v1, 2, v8
	ds_read_b32 v8, v8
	v_mov_b32_e32 v9, 0x11200
	v_lshl_add_u32 v7, v7, 2, v9
	ds_read_b32 v9, v7
	v_mov_b32_e32 v13, 0x260
	s_waitcnt lgkmcnt(1)
	v_mov_b32_dpp v7, v8 quad_perm:[1,0,3,2] row_mask:0xf bank_mask:0xf bound_ctrl:1
	v_max_f32_e32 v8, v8, v8
	v_max_f32_e32 v7, v7, v7
	v_max_f32_e32 v7, v8, v7
	v_lshlrev_b32_e32 v18, 2, v139
	v_mov_b32_e32 v19, 0
	v_mov_b32_dpp v8, v7 quad_perm:[2,3,0,1] row_mask:0xf bank_mask:0xf bound_ctrl:1
	v_max_f32_e32 v8, v8, v8
	v_max_f32_e32 v7, v7, v8
	s_mov_b32 s25, 0
	s_mov_b32 s26, s25
	v_mov_b32_dpp v8, v7 row_half_mirror row_mask:0xf bank_mask:0xf bound_ctrl:1
	v_max_f32_e32 v8, v8, v8
	v_max_f32_e32 v7, v7, v8
	s_nop 1
	v_mov_b32_dpp v8, v7 row_mirror row_mask:0xf bank_mask:0xf bound_ctrl:1
	v_max_f32_e32 v8, v8, v8
	v_max_f32_e32 v7, v7, v8
	s_nop 0
	v_readlane_b32 s4, v7, 32
	v_readlane_b32 s5, v7, 48
	v_readlane_b32 s0, v7, 0
	v_readlane_b32 s1, v7, 16
	v_max_f32_e64 v7, s5, s5
	v_max_f32_e64 v8, s4, s4
	v_max_f32_e32 v7, v8, v7
	v_mov_b32_e32 v8, s1
	v_max3_f32 v8, s0, v8, v7
	s_mov_b32 s0, 0x3f800347
	s_mov_b32 s1, 0x3f8020c5
	s_waitcnt lgkmcnt(0)
	v_pk_mul_f32 v[8:9], v[8:9], s[0:1]
	s_mov_b32 s4, 0xf800000
	v_mul_f32_e32 v7, 0x4f800000, v9
	v_cmp_gt_f32_e32 vcc, s4, v9
	s_nop 1
	v_cndmask_b32_e32 v7, v9, v7, vcc
	v_sqrt_f32_e32 v10, v7
	s_nop 0
	v_add_u32_e32 v11, -1, v10
	v_fma_f32 v12, -v11, v10, v7
	v_cmp_ge_f32_e64 s[0:1], 0, v12
	v_add_u32_e32 v12, 1, v10
	s_nop 0
	v_cndmask_b32_e64 v11, v10, v11, s[0:1]
	v_fma_f32 v10, -v12, v10, v7
	v_cmp_lt_f32_e64 s[0:1], 0, v10
	s_nop 1
	v_cndmask_b32_e64 v10, v11, v12, s[0:1]
	v_mul_f32_e32 v11, 0x37800000, v10
	v_cndmask_b32_e32 v10, v10, v11, vcc
	v_mul_f32_e32 v11, 0x4f800000, v8
	v_cmp_gt_f32_e32 vcc, s4, v8
	v_cmp_class_f32_e64 s[0:1], v7, v13
	s_nop 0
	v_cndmask_b32_e32 v11, v8, v11, vcc
	v_sqrt_f32_e32 v12, v11
	v_cndmask_b32_e64 v7, v10, v7, s[0:1]
	v_add_u32_e32 v10, -1, v12
	v_fma_f32 v15, -v10, v12, v11
	v_cmp_ge_f32_e64 s[0:1], 0, v15
	v_add_u32_e32 v15, 1, v12
	s_nop 0
	v_cndmask_b32_e64 v10, v12, v10, s[0:1]
	v_fma_f32 v12, -v15, v12, v11
	v_cmp_lt_f32_e64 s[0:1], 0, v12
	s_nop 1
	v_cndmask_b32_e64 v10, v10, v15, s[0:1]
	v_mul_f32_e32 v12, 0x37800000, v10
	v_cndmask_b32_e32 v10, v10, v12, vcc
	v_cmp_class_f32_e32 vcc, v11, v13
	s_mov_b32 s0, 0x380637bd
	s_mov_b32 s1, 0x350637bd
	v_cndmask_b32_e32 v10, v10, v11, vcc
	v_mul_f32_e32 v7, v7, v10
	v_mul_f32_e32 v7, 0x3f800347, v7
	v_pk_mul_f32 v[8:9], v[8:9], s[0:1]
	s_nop 0
	v_fmamk_f32 v7, v7, 0x3888509c, v9
	v_add_f32_e32 v7, v8, v7
	v_add_f32_e32 v7, 0xda24260, v7
	v_add_f32_e32 v6, v6, v7
	v_cmp_le_f32_e64 s[8:9], v2, v6
	v_cmp_le_f32_e64 s[6:7], v3, v6
	v_cmp_le_f32_e64 s[4:5], v4, v6
	v_lshl_add_u64 v[2:3], s[22:23], 0, v[18:19]
	s_and_b32 s19, s8, 0xffff
	s_lshl_b32 s22, s6, 16
	v_cmp_le_f32_e64 s[0:1], v5, v6
	s_or_b32 s24, s19, s22
	s_and_b32 s23, s4, 0xffff
	s_mov_b32 s22, s25
	s_or_b64 s[22:23], s[24:25], s[22:23]
	s_lshl_b32 s27, s0, 16
	s_or_b64 s[26:27], s[22:23], s[26:27]
	s_add_u32 s22, s26, -1
	s_addc_u32 s23, s27, -1
	s_and_b64 s[22:23], s[26:27], s[22:23]
	s_cmp_eq_u64 s[22:23], 0
	v_readlane_b32 s22, v14, 0
	s_cbranch_scc1 .LBB0_139
	s_lshl_b32 s19, s29, 2
	s_add_i32 s19, s19, 0x11100
	v_mov_b32_e32 v4, s19
	ds_read_b32 v4, v4
	s_mul_i32 s19, s17, 0x2040
	v_add_u32_e32 v8, s19, v135
	v_mov_b32_e32 v15, 0x7f800000
	s_waitcnt lgkmcnt(0)
	v_max_i32_e32 v4, 1, v4
	v_cvt_f64_u32_e32 v[12:13], v4
	v_div_scale_f64 v[16:17], s[30:31], v[12:13], v[12:13], 1.0
	v_rcp_f64_e32 v[20:21], v[16:17]
	v_div_scale_f64 v[22:23], vcc, 1.0, v[12:13], 1.0
	ds_read2st64_b64 v[4:7], v8 offset0:64 offset1:65
	ds_read2st64_b64 v[8:11], v8 offset0:66 offset1:67
	v_fma_f64 v[24:25], -v[16:17], v[20:21], 1.0
	v_fmac_f64_e32 v[20:21], v[20:21], v[24:25]
	v_fma_f64 v[24:25], -v[16:17], v[20:21], 1.0
	v_fmac_f64_e32 v[20:21], v[20:21], v[24:25]
	v_mul_f64 v[24:25], v[22:23], v[20:21]
	v_fma_f64 v[16:17], -v[16:17], v[24:25], v[22:23]
	v_div_fmas_f64 v[16:17], v[16:17], v[20:21], v[24:25]
	v_div_fixup_f64 v[12:13], v[16:17], v[12:13], 1.0
	s_waitcnt lgkmcnt(1)
	v_mul_f64 v[6:7], v[6:7], v[12:13]
	v_mul_f64 v[4:5], v[4:5], v[12:13]
	s_waitcnt lgkmcnt(0)
	v_mul_f64 v[8:9], v[8:9], v[12:13]
	v_mul_f64 v[10:11], v[12:13], v[10:11]
	v_mul_f64 v[12:13], v[6:7], v[6:7]
	v_fmac_f64_e32 v[12:13], v[4:5], v[4:5]
	v_fmac_f64_e32 v[12:13], v[8:9], v[8:9]
	v_fmac_f64_e32 v[12:13], v[10:11], v[10:11]
	s_nop 1
	v_mov_b32_dpp v16, v12 quad_perm:[1,0,3,2] row_mask:0xf bank_mask:0xf bound_ctrl:1
	v_mov_b32_dpp v17, v13 quad_perm:[1,0,3,2] row_mask:0xf bank_mask:0xf bound_ctrl:1
	v_add_f64 v[12:13], v[12:13], v[16:17]
	s_nop 1
	v_mov_b32_dpp v16, v12 quad_perm:[2,3,0,1] row_mask:0xf bank_mask:0xf bound_ctrl:1
	v_mov_b32_dpp v17, v13 quad_perm:[2,3,0,1] row_mask:0xf bank_mask:0xf bound_ctrl:1
	v_add_f64 v[12:13], v[12:13], v[16:17]
	s_nop 1
	v_mov_b32_dpp v16, v12 row_half_mirror row_mask:0xf bank_mask:0xf bound_ctrl:1
	v_mov_b32_dpp v17, v13 row_half_mirror row_mask:0xf bank_mask:0xf bound_ctrl:1
	v_add_f64 v[12:13], v[12:13], v[16:17]
	s_nop 1
	v_mov_b32_dpp v16, v12 row_mirror row_mask:0xf bank_mask:0xf bound_ctrl:1
	v_mov_b32_dpp v17, v13 row_mirror row_mask:0xf bank_mask:0xf bound_ctrl:1
	v_add_f64 v[12:13], v[12:13], v[16:17]
	s_nop 0
	v_readlane_b32 s19, v13, 16
	v_readlane_b32 s23, v12, 16
	v_readlane_b32 s31, v13, 0
	v_readlane_b32 s30, v12, 0
	v_mov_b32_e32 v16, s23
	v_mov_b32_e32 v17, s19
	v_readlane_b32 s19, v13, 48
	v_readlane_b32 s23, v12, 48
	v_add_f64 v[16:17], s[30:31], v[16:17]
	v_readlane_b32 s31, v13, 32
	v_readlane_b32 s30, v12, 32
	v_mov_b32_e32 v12, s23
	v_mov_b32_e32 v13, s19
	v_add_f64 v[12:13], s[30:31], v[12:13]
	v_add_f64 v[12:13], v[16:17], v[12:13]

.LBB0_139:
.Lpad_7:
	s_cbranch_execz .Lwret_7
	s_lshr_b32 s8, s8, 16
	s_and_b32 s19, s6, 0xffff0000
	s_mov_b32 s25, 0
	s_lshl_b64 s[26:27], s[4:5], 16
	s_or_b32 s24, s19, s8
	s_and_b32 s27, s27, 0xffff
	s_mov_b32 s26, s25
	s_or_b64 s[26:27], s[24:25], s[26:27]
	s_and_b32 s31, s0, 0xffff0000
	s_mov_b32 s30, s25
	s_or_b64 s[26:27], s[26:27], s[30:31]
	s_add_u32 s30, s26, -1
	s_addc_u32 s31, s27, -1
	s_and_b64 s[30:31], s[26:27], s[30:31]
	s_cmp_eq_u64 s[30:31], 0
	v_readlane_b32 s8, v14, 16
	s_cbranch_scc1 .LBB0_142
	s_or_b32 s19, s29, 1
	s_lshl_b32 s23, s19, 2
	s_add_i32 s23, s23, 0x11100
	v_mov_b32_e32 v4, s23
	ds_read_b32 v4, v4
	s_mulk_i32 s19, 0x810
	v_add_u32_e32 v8, s19, v135
	v_mov_b32_e32 v15, 0x7f800000
	s_waitcnt lgkmcnt(0)
	v_max_i32_e32 v4, 1, v4
	v_cvt_f64_u32_e32 v[12:13], v4
	v_div_scale_f64 v[16:17], s[30:31], v[12:13], v[12:13], 1.0
	v_rcp_f64_e32 v[20:21], v[16:17]
	v_div_scale_f64 v[22:23], vcc, 1.0, v[12:13], 1.0
	ds_read2st64_b64 v[4:7], v8 offset0:64 offset1:65
	ds_read2st64_b64 v[8:11], v8 offset0:66 offset1:67
	v_fma_f64 v[24:25], -v[16:17], v[20:21], 1.0
	v_fmac_f64_e32 v[20:21], v[20:21], v[24:25]
	v_fma_f64 v[24:25], -v[16:17], v[20:21], 1.0
	v_fmac_f64_e32 v[20:21], v[20:21], v[24:25]
	v_mul_f64 v[24:25], v[22:23], v[20:21]
	v_fma_f64 v[16:17], -v[16:17], v[24:25], v[22:23]
	v_div_fmas_f64 v[16:17], v[16:17], v[20:21], v[24:25]
	v_div_fixup_f64 v[12:13], v[16:17], v[12:13], 1.0
	s_waitcnt lgkmcnt(1)
	v_mul_f64 v[6:7], v[6:7], v[12:13]
	v_mul_f64 v[4:5], v[4:5], v[12:13]
	s_waitcnt lgkmcnt(0)
	v_mul_f64 v[8:9], v[8:9], v[12:13]
	v_mul_f64 v[10:11], v[12:13], v[10:11]
	v_mul_f64 v[12:13], v[6:7], v[6:7]
	v_fmac_f64_e32 v[12:13], v[4:5], v[4:5]
	v_fmac_f64_e32 v[12:13], v[8:9], v[8:9]
	v_fmac_f64_e32 v[12:13], v[10:11], v[10:11]
	s_nop 1
	v_mov_b32_dpp v16, v12 quad_perm:[1,0,3,2] row_mask:0xf bank_mask:0xf bound_ctrl:1
	v_mov_b32_dpp v17, v13 quad_perm:[1,0,3,2] row_mask:0xf bank_mask:0xf bound_ctrl:1
	v_add_f64 v[12:13], v[12:13], v[16:17]
	s_nop 1
	v_mov_b32_dpp v16, v12 quad_perm:[2,3,0,1] row_mask:0xf bank_mask:0xf bound_ctrl:1
	v_mov_b32_dpp v17, v13 quad_perm:[2,3,0,1] row_mask:0xf bank_mask:0xf bound_ctrl:1
	v_add_f64 v[12:13], v[12:13], v[16:17]
	s_nop 1
	v_mov_b32_dpp v16, v12 row_half_mirror row_mask:0xf bank_mask:0xf bound_ctrl:1
	v_mov_b32_dpp v17, v13 row_half_mirror row_mask:0xf bank_mask:0xf bound_ctrl:1
	v_add_f64 v[12:13], v[12:13], v[16:17]
	s_nop 1
	v_mov_b32_dpp v16, v12 row_mirror row_mask:0xf bank_mask:0xf bound_ctrl:1
	v_mov_b32_dpp v17, v13 row_mirror row_mask:0xf bank_mask:0xf bound_ctrl:1
	v_add_f64 v[12:13], v[12:13], v[16:17]
	s_nop 0
	v_readlane_b32 s19, v13, 16
	v_readlane_b32 s23, v12, 16
	v_readlane_b32 s31, v13, 0
	v_readlane_b32 s30, v12, 0
	v_mov_b32_e32 v16, s23
	v_mov_b32_e32 v17, s19
	v_readlane_b32 s19, v13, 48
	v_readlane_b32 s23, v12, 48
	v_add_f64 v[16:17], s[30:31], v[16:17]
	v_readlane_b32 s31, v13, 32
	v_readlane_b32 s30, v12, 32
	v_mov_b32_e32 v12, s23
	v_mov_b32_e32 v13, s19
	v_add_f64 v[12:13], s[30:31], v[12:13]
	v_add_f64 v[12:13], v[16:17], v[12:13]

.LBB0_142:
.Lpad_8:
	s_cbranch_execz .Lwret_8
	s_mov_b32 s25, 0
	s_lshr_b64 s[26:27], s[6:7], 16
	s_and_b32 s24, s9, 0xffff
	s_and_b32 s26, s26, 0xffff0000
	s_mov_b32 s27, s25
	s_or_b64 s[26:27], s[26:27], s[24:25]
	s_and_b32 s31, s5, 0xffff
	s_mov_b32 s30, s25
	s_or_b64 s[26:27], s[26:27], s[30:31]
	s_lshl_b64 s[30:31], s[0:1], 16
	s_and_b32 s31, s31, 0xffff0000
	s_mov_b32 s30, s25
	s_or_b64 s[26:27], s[26:27], s[30:31]
	s_add_u32 s30, s26, -1
	s_addc_u32 s31, s27, -1
	s_and_b64 s[30:31], s[26:27], s[30:31]
	s_cmp_eq_u64 s[30:31], 0
	v_readlane_b32 s0, v14, 32
	s_cbranch_scc1 .LBB0_145
	s_or_b32 s6, s29, 2
	s_lshl_b32 s19, s6, 2
	s_add_i32 s19, s19, 0x11100
	v_mov_b32_e32 v4, s19
	ds_read_b32 v4, v4
	s_mulk_i32 s6, 0x810
	v_add_u32_e32 v8, s6, v135
	v_mov_b32_e32 v15, 0x7f800000
	s_waitcnt lgkmcnt(0)
	v_max_i32_e32 v4, 1, v4
	v_cvt_f64_u32_e32 v[12:13], v4
	v_div_scale_f64 v[16:17], s[30:31], v[12:13], v[12:13], 1.0
	v_rcp_f64_e32 v[20:21], v[16:17]
	v_div_scale_f64 v[22:23], vcc, 1.0, v[12:13], 1.0
	ds_read2st64_b64 v[4:7], v8 offset0:64 offset1:65
	ds_read2st64_b64 v[8:11], v8 offset0:66 offset1:67
	v_fma_f64 v[24:25], -v[16:17], v[20:21], 1.0
	v_fmac_f64_e32 v[20:21], v[20:21], v[24:25]
	v_fma_f64 v[24:25], -v[16:17], v[20:21], 1.0
	v_fmac_f64_e32 v[20:21], v[20:21], v[24:25]
	v_mul_f64 v[24:25], v[22:23], v[20:21]
	v_fma_f64 v[16:17], -v[16:17], v[24:25], v[22:23]
	v_div_fmas_f64 v[16:17], v[16:17], v[20:21], v[24:25]
	v_div_fixup_f64 v[12:13], v[16:17], v[12:13], 1.0
	s_waitcnt lgkmcnt(1)
	v_mul_f64 v[6:7], v[6:7], v[12:13]
	v_mul_f64 v[4:5], v[4:5], v[12:13]
	s_waitcnt lgkmcnt(0)
	v_mul_f64 v[8:9], v[8:9], v[12:13]
	v_mul_f64 v[10:11], v[12:13], v[10:11]
	v_mul_f64 v[12:13], v[6:7], v[6:7]
	v_fmac_f64_e32 v[12:13], v[4:5], v[4:5]
	v_fmac_f64_e32 v[12:13], v[8:9], v[8:9]
	v_fmac_f64_e32 v[12:13], v[10:11], v[10:11]
	s_nop 1
	v_mov_b32_dpp v16, v12 quad_perm:[1,0,3,2] row_mask:0xf bank_mask:0xf bound_ctrl:1
	v_mov_b32_dpp v17, v13 quad_perm:[1,0,3,2] row_mask:0xf bank_mask:0xf bound_ctrl:1
	v_add_f64 v[12:13], v[12:13], v[16:17]
	s_nop 1
	v_mov_b32_dpp v16, v12 quad_perm:[2,3,0,1] row_mask:0xf bank_mask:0xf bound_ctrl:1
	v_mov_b32_dpp v17, v13 quad_perm:[2,3,0,1] row_mask:0xf bank_mask:0xf bound_ctrl:1
	v_add_f64 v[12:13], v[12:13], v[16:17]
	s_nop 1
	v_mov_b32_dpp v16, v12 row_half_mirror row_mask:0xf bank_mask:0xf bound_ctrl:1
	v_mov_b32_dpp v17, v13 row_half_mirror row_mask:0xf bank_mask:0xf bound_ctrl:1
	v_add_f64 v[12:13], v[12:13], v[16:17]
	s_nop 1
	v_mov_b32_dpp v16, v12 row_mirror row_mask:0xf bank_mask:0xf bound_ctrl:1
	v_mov_b32_dpp v17, v13 row_mirror row_mask:0xf bank_mask:0xf bound_ctrl:1
	v_add_f64 v[12:13], v[12:13], v[16:17]
	s_nop 0
	v_readlane_b32 s6, v13, 16
	v_readlane_b32 s19, v12, 16
	v_readlane_b32 s31, v13, 0
	v_readlane_b32 s30, v12, 0
	v_mov_b32_e32 v16, s19
	v_mov_b32_e32 v17, s6
	v_readlane_b32 s6, v13, 48
	v_readlane_b32 s19, v12, 48
	v_add_f64 v[16:17], s[30:31], v[16:17]
	v_readlane_b32 s31, v13, 32
	v_readlane_b32 s30, v12, 32
	v_mov_b32_e32 v12, s19
	v_mov_b32_e32 v13, s6
	v_add_f64 v[12:13], s[30:31], v[12:13]
	v_add_f64 v[12:13], v[16:17], v[12:13]

.LBB0_145:
.Lpad_9:
	s_cbranch_execz .Lwret_9
	s_mov_b32 s25, 0
	s_lshr_b32 s24, s9, 16
	s_and_b32 s6, s7, 0xffff0000
	s_mov_b32 s7, s25
	s_lshr_b64 s[4:5], s[4:5], 16
	s_or_b64 s[6:7], s[6:7], s[24:25]
	s_mov_b32 s4, s25
	s_or_b64 s[4:5], s[6:7], s[4:5]
	s_and_b32 s7, s1, 0xffff0000
	s_mov_b32 s6, s25
	s_or_b64 s[6:7], s[4:5], s[6:7]
	s_add_u32 s4, s6, -1
	s_addc_u32 s5, s7, -1
	s_and_b64 s[4:5], s[6:7], s[4:5]
	s_cmp_eq_u64 s[4:5], 0
	v_readlane_b32 s4, v14, 48
	s_cbranch_scc1 .LBB0_148
	s_or_b32 s1, s29, 3
	s_lshl_b32 s5, s1, 2
	s_add_i32 s5, s5, 0x11100
	v_mov_b32_e32 v4, s5
	ds_read_b32 v4, v4
	s_mulk_i32 s1, 0x810
	v_add_u32_e32 v8, s1, v135
	s_waitcnt lgkmcnt(0)
	v_max_i32_e32 v4, 1, v4
	v_cvt_f64_u32_e32 v[12:13], v4
	v_div_scale_f64 v[14:15], s[26:27], v[12:13], v[12:13], 1.0
	v_rcp_f64_e32 v[16:17], v[14:15]
	v_div_scale_f64 v[20:21], vcc, 1.0, v[12:13], 1.0
	ds_read2st64_b64 v[4:7], v8 offset0:64 offset1:65
	ds_read2st64_b64 v[8:11], v8 offset0:66 offset1:67
	v_fma_f64 v[22:23], -v[14:15], v[16:17], 1.0
	v_fmac_f64_e32 v[16:17], v[16:17], v[22:23]
	v_fma_f64 v[22:23], -v[14:15], v[16:17], 1.0
	v_fmac_f64_e32 v[16:17], v[16:17], v[22:23]
	v_mul_f64 v[22:23], v[20:21], v[16:17]
	v_fma_f64 v[14:15], -v[14:15], v[22:23], v[20:21]
	v_div_fmas_f64 v[14:15], v[14:15], v[16:17], v[22:23]
	v_div_fixup_f64 v[12:13], v[14:15], v[12:13], 1.0
	s_waitcnt lgkmcnt(1)
	v_mul_f64 v[6:7], v[6:7], v[12:13]
	v_mul_f64 v[4:5], v[4:5], v[12:13]
	s_waitcnt lgkmcnt(0)
	v_mul_f64 v[8:9], v[8:9], v[12:13]
	v_mul_f64 v[10:11], v[12:13], v[10:11]
	v_mul_f64 v[12:13], v[6:7], v[6:7]
	v_fmac_f64_e32 v[12:13], v[4:5], v[4:5]
	v_fmac_f64_e32 v[12:13], v[8:9], v[8:9]
	v_fmac_f64_e32 v[12:13], v[10:11], v[10:11]
	s_nop 1
	v_mov_b32_dpp v14, v12 quad_perm:[1,0,3,2] row_mask:0xf bank_mask:0xf bound_ctrl:1
	v_mov_b32_dpp v15, v13 quad_perm:[1,0,3,2] row_mask:0xf bank_mask:0xf bound_ctrl:1
	v_add_f64 v[12:13], v[12:13], v[14:15]
	s_nop 1
	v_mov_b32_dpp v14, v12 quad_perm:[2,3,0,1] row_mask:0xf bank_mask:0xf bound_ctrl:1
	v_mov_b32_dpp v15, v13 quad_perm:[2,3,0,1] row_mask:0xf bank_mask:0xf bound_ctrl:1
	v_add_f64 v[12:13], v[12:13], v[14:15]
	s_nop 1
	v_mov_b32_dpp v14, v12 row_half_mirror row_mask:0xf bank_mask:0xf bound_ctrl:1
	v_mov_b32_dpp v15, v13 row_half_mirror row_mask:0xf bank_mask:0xf bound_ctrl:1
	v_add_f64 v[12:13], v[12:13], v[14:15]
	s_nop 1
	v_mov_b32_dpp v14, v12 row_mirror row_mask:0xf bank_mask:0xf bound_ctrl:1
	v_mov_b32_dpp v15, v13 row_mirror row_mask:0xf bank_mask:0xf bound_ctrl:1
	v_add_f64 v[12:13], v[12:13], v[14:15]
	s_nop 0
	v_readlane_b32 s1, v13, 16
	v_readlane_b32 s5, v12, 16
	v_readlane_b32 s27, v13, 0
	v_readlane_b32 s26, v12, 0
	v_mov_b32_e32 v14, s5
	v_mov_b32_e32 v15, s1
	v_readlane_b32 s1, v13, 48
	v_readlane_b32 s5, v12, 48
	v_add_f64 v[14:15], s[26:27], v[14:15]
	v_readlane_b32 s27, v13, 32
	v_readlane_b32 s26, v12, 32
	v_mov_b32_e32 v12, s5
	v_mov_b32_e32 v13, s1
	v_add_f64 v[12:13], s[26:27], v[12:13]
	v_add_f64 v[12:13], v[14:15], v[12:13]
	v_mov_b32_e32 v14, 0x7f800000

.LBB0_148:
.Lpad_10:
	s_cbranch_execz .Lwret_10
	s_ashr_i32 s23, s22, 31
	s_lshl_b64 s[6:7], s[22:23], 10
	s_ashr_i32 s9, s8, 31
	v_lshl_add_u64 v[4:5], v[2:3], 0, s[6:7]
	s_lshl_b64 s[6:7], s[8:9], 10
	s_ashr_i32 s1, s0, 31
	v_lshl_add_u64 v[6:7], v[2:3], 0, s[6:7]
	s_lshl_b64 s[6:7], s[0:1], 10
	s_ashr_i32 s5, s4, 31
	global_load_dwordx4 v[14:17], v[4:5], off
	global_load_dwordx4 v[10:13], v[6:7], off
	v_lshl_add_u64 v[20:21], v[2:3], 0, s[6:7]
	s_lshl_b64 s[6:7], s[4:5], 10
	v_lshl_add_u64 v[22:23], v[2:3], 0, s[6:7]
	global_load_dwordx4 v[6:9], v[20:21], off
	global_load_dwordx4 v[2:5], v[22:23], off
	s_mul_i32 s1, s17, 0x1020
	v_mov_b32_e32 v19, 0
	v_lshl_add_u32 v1, v1, 2, s1
	v_lshl_add_u64 v[20:21], s[20:21], 0, v[18:19]
	v_add_u32_e32 v18, 8, v1
	v_add_u32_e32 v22, 16, v1
	ds_read2st64_b32 v[36:37], v1 offset1:1
	ds_read2st64_b32 v[34:35], v1 offset0:2 offset1:3
	v_add_u32_e32 v1, 24, v1
	ds_read2st64_b32 v[32:33], v18 offset0:4 offset1:5
	ds_read2st64_b32 v[30:31], v18 offset0:6 offset1:7
	ds_read2st64_b32 v[28:29], v22 offset0:8 offset1:9
	ds_read2st64_b32 v[26:27], v22 offset0:10 offset1:11
	ds_read2st64_b32 v[24:25], v1 offset0:12 offset1:13
	ds_read2st64_b32 v[22:23], v1 offset0:14 offset1:15
	s_lshl_b32 s5, s18, 9
	s_or_b32 s1, s5, s28
	s_waitcnt lgkmcnt(7)
	v_add_f32_e64 v1, |v36|, |v37|
	s_mov_b32 s7, 0
	s_add_i32 s6, s1, s29
	s_waitcnt lgkmcnt(6)
	v_add_f32_e64 v1, |v34|, v1
	s_lshl_b64 s[18:19], s[6:7], 10
	v_add_f32_e64 v1, |v35|, v1
	v_lshl_add_u64 v[42:43], v[20:21], 0, s[18:19]
	v_cmp_lt_f32_e32 vcc, 0, v1
	s_waitcnt vmcnt(3)
	v_pk_add_f32 v[38:39], v[14:15], v[36:37] neg_lo:[0,1] neg_hi:[0,1]
	v_pk_add_f32 v[40:41], v[16:17], v[34:35] neg_lo:[0,1] neg_hi:[0,1]
	v_pk_add_f32 v[38:39], v[36:37], v[38:39]
	v_pk_add_f32 v[40:41], v[34:35], v[40:41]
	global_store_dwordx4 v[42:43], v[38:41], off nt
	s_cbranch_vccz .LBB0_150
	v_pk_add_f32 v[14:15], v[36:37], v[14:15] neg_lo:[0,1] neg_hi:[0,1]
	v_pk_add_f32 v[16:17], v[34:35], v[16:17] neg_lo:[0,1] neg_hi:[0,1]
	v_pk_mul_f32 v[14:15], v[14:15], v[14:15]
	v_pk_mul_f32 v[16:17], v[16:17], v[16:17]
	v_add_f32_e32 v1, v14, v15
	v_add_f32_e32 v1, v1, v16
	v_add_f32_e32 v19, v1, v17
	s_mov_b32 s7, 1
.LBB0_150:
.Lpad_11:
	s_cbranch_execz .Lwret_11
	s_and_saveexec_b64 s[18:19], s[2:3]
	s_lshl_b32 s5, s29, 2
	s_add_i32 s5, s5, 0x11160
	v_mov_b32_e32 v1, s5
	v_mov_b32_e32 v14, s22
	ds_write_b32 v1, v14
	s_or_b64 exec, exec, s[18:19]
	s_or_b32 s5, s29, 1
	s_waitcnt lgkmcnt(5)
	v_add_f32_e64 v1, |v32|, |v33|
	s_add_i32 s18, s1, s5
	s_mov_b32 s19, 0
	s_waitcnt lgkmcnt(4)
	v_add_f32_e64 v1, |v30|, v1
	s_waitcnt vmcnt(3)
	v_pk_add_f32 v[14:15], v[10:11], v[32:33] neg_lo:[0,1] neg_hi:[0,1]
	v_pk_add_f32 v[16:17], v[12:13], v[30:31] neg_lo:[0,1] neg_hi:[0,1]
	s_lshl_b64 s[18:19], s[18:19], 10
	v_add_f32_e64 v1, |v31|, v1
	v_pk_add_f32 v[14:15], v[32:33], v[14:15]
	v_pk_add_f32 v[16:17], v[30:31], v[16:17]
	v_lshl_add_u64 v[34:35], v[20:21], 0, s[18:19]
	v_cmp_lt_f32_e32 vcc, 0, v1
	global_store_dwordx4 v[34:35], v[14:17], off nt
	s_cbranch_vccz .LBB0_154
	v_pk_add_f32 v[10:11], v[32:33], v[10:11] neg_lo:[0,1] neg_hi:[0,1]
	v_pk_add_f32 v[12:13], v[30:31], v[12:13] neg_lo:[0,1] neg_hi:[0,1]
	v_pk_mul_f32 v[10:11], v[10:11], v[10:11]
	v_pk_mul_f32 v[12:13], v[12:13], v[12:13]
	v_add_f32_e32 v1, v10, v11
	v_add_f32_e32 v1, v1, v12
	v_add_f32_e32 v1, v1, v13
	v_add_f32_e32 v19, v19, v1
	s_add_i32 s7, s7, 1
.LBB0_154:
.Lpad_12:
	s_cbranch_execz .Lwret_12
	s_and_saveexec_b64 s[18:19], s[2:3]
	s_lshl_b32 s5, s5, 2
	s_add_i32 s5, s5, 0x11160
	v_mov_b32_e32 v1, s5
	v_mov_b32_e32 v10, s8
	ds_write_b32 v1, v10
	s_or_b64 exec, exec, s[18:19]
	s_or_b32 s5, s29, 2
	s_waitcnt lgkmcnt(3)
	v_add_f32_e64 v1, |v28|, |v29|
	s_add_i32 s8, s1, s5
	s_mov_b32 s9, 0
	s_waitcnt lgkmcnt(2)
	v_add_f32_e64 v1, |v26|, v1
	s_waitcnt vmcnt(3)
	v_pk_add_f32 v[10:11], v[6:7], v[28:29] neg_lo:[0,1] neg_hi:[0,1]
	v_pk_add_f32 v[12:13], v[8:9], v[26:27] neg_lo:[0,1] neg_hi:[0,1]
	s_lshl_b64 s[8:9], s[8:9], 10
	v_add_f32_e64 v1, |v27|, v1
	v_pk_add_f32 v[10:11], v[28:29], v[10:11]
	v_pk_add_f32 v[12:13], v[26:27], v[12:13]
	v_lshl_add_u64 v[14:15], v[20:21], 0, s[8:9]
	v_cmp_lt_f32_e32 vcc, 0, v1
	global_store_dwordx4 v[14:15], v[10:13], off nt
	s_cbranch_vccz .LBB0_158
	v_pk_add_f32 v[6:7], v[28:29], v[6:7] neg_lo:[0,1] neg_hi:[0,1]
	v_pk_add_f32 v[8:9], v[26:27], v[8:9] neg_lo:[0,1] neg_hi:[0,1]
	v_pk_mul_f32 v[6:7], v[6:7], v[6:7]
	v_pk_mul_f32 v[8:9], v[8:9], v[8:9]
	v_add_f32_e32 v1, v6, v7
	v_add_f32_e32 v1, v1, v8
	v_add_f32_e32 v1, v1, v9
	v_add_f32_e32 v19, v19, v1
	s_add_i32 s7, s7, 1
.LBB0_158:
.Lpad_13:
	s_cbranch_execz .Lwret_13
	s_and_saveexec_b64 s[8:9], s[2:3]
	s_lshl_b32 s5, s5, 2
	s_add_i32 s5, s5, 0x11160
	v_mov_b32_e32 v1, s5
	v_mov_b32_e32 v6, s0
	ds_write_b32 v1, v6
	s_or_b64 exec, exec, s[8:9]
	s_or_b32 s5, s29, 3
	s_waitcnt lgkmcnt(1)
	v_add_f32_e64 v1, |v24|, |v25|
	s_add_i32 s0, s1, s5
	s_mov_b32 s1, 0
	s_waitcnt lgkmcnt(0)
	v_add_f32_e64 v1, |v22|, v1
	s_waitcnt vmcnt(3)
	v_pk_add_f32 v[6:7], v[2:3], v[24:25] neg_lo:[0,1] neg_hi:[0,1]
	v_pk_add_f32 v[8:9], v[4:5], v[22:23] neg_lo:[0,1] neg_hi:[0,1]
	s_lshl_b64 s[0:1], s[0:1], 10
	v_add_f32_e64 v1, |v23|, v1
	v_pk_add_f32 v[6:7], v[24:25], v[6:7]
	v_pk_add_f32 v[8:9], v[22:23], v[8:9]
	v_lshl_add_u64 v[10:11], v[20:21], 0, s[0:1]
	v_cmp_lt_f32_e32 vcc, 0, v1
	global_store_dwordx4 v[10:11], v[6:9], off nt
	s_cbranch_vccz .LBB0_162
	v_pk_add_f32 v[2:3], v[24:25], v[2:3] neg_lo:[0,1] neg_hi:[0,1]
	v_pk_add_f32 v[4:5], v[22:23], v[4:5] neg_lo:[0,1] neg_hi:[0,1]
	v_pk_mul_f32 v[2:3], v[2:3], v[2:3]
	v_pk_mul_f32 v[4:5], v[4:5], v[4:5]
	v_add_f32_e32 v1, v2, v3
	v_add_f32_e32 v1, v1, v4
	v_add_f32_e32 v1, v1, v5
	v_add_f32_e32 v19, v19, v1
	s_add_i32 s7, s7, 1
.LBB0_162:
.Lpad_14:
	s_cbranch_execz .Lwret_14
	s_and_saveexec_b64 s[0:1], s[2:3]
	s_lshl_b32 s5, s5, 2
	s_add_i32 s5, s5, 0x11160
	v_mov_b32_e32 v1, s5
	v_mov_b32_e32 v2, s4
	ds_write_b32 v1, v2
	s_or_b64 exec, exec, s[0:1]
	v_add_f32_dpp v1, v19, v19 quad_perm:[1,0,3,2] row_mask:0xf bank_mask:0xf bound_ctrl:1
	s_nop 1
	v_add_f32_dpp v1, v1, v1 quad_perm:[2,3,0,1] row_mask:0xf bank_mask:0xf bound_ctrl:1
	s_nop 1
	v_add_f32_dpp v1, v1, v1 row_half_mirror row_mask:0xf bank_mask:0xf bound_ctrl:1
	s_nop 1
	v_add_f32_dpp v1, v1, v1 row_mirror row_mask:0xf bank_mask:0xf bound_ctrl:1
	s_nop 0
	v_readlane_b32 s4, v1, 0
	v_readlane_b32 s6, v1, 16
	v_readlane_b32 s5, v1, 32
	v_readlane_b32 s8, v1, 48
	s_and_saveexec_b64 s[0:1], s[2:3]
	s_cbranch_execz .LBB0_166
	v_mov_b32_e32 v1, s6
	v_mov_b32_e32 v2, s8
	s_lshl_b32 s3, s17, 3
	v_add_f32_e32 v1, s4, v1
	v_add_f32_e32 v2, s5, v2
	s_add_i32 s3, s3, 0x111a0
	v_add_f32_e32 v1, v1, v2
	s_add_i32 s2, s29, 0x11150
	v_cvt_f64_f32_e32 v[2:3], v1
	v_mov_b32_e32 v1, s3
	ds_write_b64 v1, v[2:3]
	v_mov_b32_e32 v1, s2
	v_mov_b32_e32 v2, s7
	ds_write_b32 v1, v2
.LBB0_166:
	s_or_b64 exec, exec, s[0:1]
	v_cmp_gt_u32_e32 vcc, 64, v0
	s_waitcnt lgkmcnt(0)
	s_barrier
.Lpad_15:
	s_cbranch_execz .Lwret_15
	s_and_saveexec_b64 s[0:1], vcc
	s_cbranch_execnz .LBB0_169
	s_or_b64 exec, exec, s[0:1]
	v_cmp_eq_u32_e32 vcc, 64, v0
	s_and_saveexec_b64 s[0:1], vcc
	s_cbranch_execnz .LBB0_170
